# PEER static priority on the older half (waves 0-3) instead of waves 4-7
# speedup vs baseline: 1.0009x; 1.0009x over previous
.Le1w_first:
	v_readfirstlane_b32 s98, v0
	s_nop 3
	s_cmp_ge_u32 s98, 0x100
	s_cbranch_scc1 .Lpr_e1
	s_setprio 1
